# v38 + FFN-up conversion hook trigger made uniform per XCD ((bid&7)%5) so the 32 workgroups sharing an L2 stay in K lockstep
# baseline (speedup 1.0000x reference)
; #define PG8_WAIT_V(n) asm volatile("s_waitcnt vmcnt(" #n ")" ::: "memory")
; #define PG8_BAR __builtin_amdgcn_s_barrier()
; template <class Epi, class Sched, bool ALIGN_EPI = false, bool SP2 = false>
; __device__ __forceinline__ void gemm_phase(PG8_LAS unsigned char* lds, const Gemm g, const Sched& S, const Epi& E, const int tid) {
;     ...
;     for (int i = 0; i < 2; ++i) { int R, C; stage_rc(tid * 16 + i * 8192, R, C); const int Rb = Epi::PERM ? ((R & ~31) + perm32(R & 31)) : R;
;         voffA[i] = (unsigned)(R * K + C) * 2u; voffB[i] = (unsigned)(Rb * K + C) * 2u; }
;     const size_t kstep = (size_t)(BK * 2);
;     const size_t hstep = (size_t)HALF * K * 2;
;     const size_t tstep = 2 * hstep;
;     const unsigned ldsw = (unsigned)wid * 1024u;
;     const int aoff = lds_byte(wr * 64 + fr, fq * 8), boff = lds_byte(wc * 32 + fr, fq * 8);
;     ...
;     Unit cur, nxt; int ui = 0;
;     if (!S.next(0, cur)) return;
;     f32x4 acc[2][2][4][2];
; #pragma unroll
;     for (int a = 0; a < 2; ++a)
; #pragma unroll
;         for (int b = 0; b < 2; ++b)
; #pragma unroll
;             for (int m = 0; m < 4; ++m)
; #pragma unroll
;                 for (int n = 0; n < 2; ++n) acc[a][b][m][n] = (f32x4){0.f, 0.f, 0.f, 0.f};
;     bf16x8 At[4][2], B0[2][2], B1[2][2];
;     const char* cA = (const char*)g.A + (size_t)cur.pm * tstep + (size_t)cur.k0 * 2; const char* cB = (const char*)g.Bt + (size_t)cur.pn * tstep + (size_t)cur.k0 * 2; nt = cur.nt;
;     S.a_ready(cur);
;     if constexpr (SP2) {
;         PG8_STAGE(PG8_SB(0, 0), cB, voffB); PG8_STAGE(PG8_SB(0, 1), cB + hstep, voffB); PG8_STAGE(PG8_SA(0, 0), cA, voffA); PG8_STAGE(PG8_SA(0, 1), cA + hstep, voffA);
;         if (wr == 1) PG8_BAR;
;         PG8_WAIT_V(2); PG8_BAR;
;         PG8_STAGE(PG8_SB(1, 0), cB + kstep, voffB); PG8_STAGE(PG8_SA(1, 0), cA + kstep, voffA); PG8_STAGE(PG8_SB(1, 1), cB + hstep + kstep, voffB);
; __device__ __forceinline__ void ph_ffnup(LAS unsigned char* lds, unsigned char* ws, int bid, int tid) {
;     pg8::Gemm g{(const pg8::bf16_t*)(ws + WS_XN), (const pg8::bf16_t*)(ws + WS_FUP), MR, 2 * FF, D};
;     pg8::MixOrder<2 * FF / 256, D / 64, 1, D, 1, 0, true> S{NMT, bid, 0, 0, pg8::ConvHook{CT_INPROJ0_HI, CT_FFNUP_HI, bid % 5}};
;     pg8::EpiSwiglu E{(pg8::bf16_t*)(ws + WS_ACT), FF, 2 * FF / 256};
;     pg8::gemm_phase<pg8::EpiSwiglu, decltype(S), true, true>(lds + RING_OFF, g, S, E, tid);
.LBB0_2276:
	s_and_b32 s100, s27, 7
	s_mul_hi_i32 s5, s100, 0x66666667
	s_lshr_b32 s12, s5, 31
	s_ashr_i32 s5, s5, 1
	s_add_i32 s5, s5, s12
	v_lshrrev_b32_e32 v18, 1, v154
	s_mul_i32 s5, s5, 5
	v_and_b32_e32 v18, 24, v18
	s_sub_i32 s71, s100, s5
	v_and_b32_e32 v17, 15, v154
	v_lshlrev_b32_e32 v19, 1, v18
	s_add_u32 s8, s8, 0x48900000
	v_lshl_or_b32 v155, s10, 6, v17
	v_lshl_or_b32 v17, v17, 6, v19
	v_lshlrev_b32_e32 v19, 2, v154
	s_addc_u32 s9, s9, 0
	s_lshl_b32 s5, s10, 13
	v_and_b32_e32 v19, 32, v19
	v_bitop3_b32 v20, v17, s5, v19 bitop3:0xde
	s_lshl_b32 s5, s11, 5
	s_and_b32 s5, s5, 0x60
	s_add_i32 m0, s65, 0x18000
	v_lshl_add_u64 v[8:9], v[8:9], 0, s[34:35]
	s_lshl_b32 s10, s5, 7
	s_waitcnt vmcnt(2)
	s_barrier
	global_load_lds_dwordx4 v[8:9], off
	v_lshl_add_u64 v[6:7], v[6:7], 0, s[34:35]
	s_add_i32 m0, s65, 0x1a000
	s_add_i32 s72, s65, 0x8000
	s_add_i32 s73, s65, 0xa000
	v_bitop3_b32 v156, s10, v17, v19 bitop3:0xf6
	global_load_lds_dwordx4 v[6:7], off
	v_lshl_add_u64 v[2:3], v[2:3], 0, s[34:35]
	s_mov_b32 m0, s72
	s_add_u32 s10, s6, 0x80080
	global_load_lds_dwordx4 v[2:3], off
	v_lshl_add_u64 v[2:3], v[4:5], 0, s[34:35]
	s_mov_b32 m0, s73
	s_addc_u32 s11, s7, 0
	global_load_lds_dwordx4 v[2:3], off
	s_add_i32 m0, s65, 0x1c000
	v_lshl_add_u64 v[2:3], s[10:11], 0, v[136:137]
	global_load_lds_dwordx4 v[2:3], off
	s_add_i32 m0, s65, 0x1e000
	v_lshl_add_u64 v[2:3], s[10:11], 0, v[140:141]
	s_cmpk_lt_u32 s2, 0x100
	global_load_lds_dwordx4 v[2:3], off
	s_cselect_b64 s[10:11], -1, 0
	v_and_b32_e32 v2, 63, v154
	v_readlane_b32 s2, v253, 55
	s_add_i32 s74, s27, 0x10ca
	v_lshlrev_b32_e32 v157, 2, v2
	v_lshl_add_u32 v235, v2, 8, s2
	v_bitop3_b32 v2, v16, 48, v154 bitop3:0x48
	s_lshl_b32 s12, s74, 1
	v_add_u32_e32 v161, s2, v2
	s_add_i32 s2, s12, 0xfffff000
	s_mul_hi_i32 s13, s2, 0x92492493
	s_add_i32 s13, s13, s2
	s_lshr_b32 s15, s13, 31
	s_ashr_i32 s13, s13, 12
	s_add_i32 s13, s13, s15
	s_mulk_i32 s13, 0x1c00
	s_sub_i32 s2, s2, s13
	s_sext_i32_i16 s13, s2
	s_mulk_i32 s13, 0x4925
	s_lshr_b32 s15, s13, 31
	s_ashr_i32 s13, s13, 24
	s_add_i32 s13, s13, s15
	s_mul_i32 s15, s13, 0x380
	s_sub_i32 s15, s2, s15
	s_sext_i32_i16 s16, s15
	s_lshr_b32 s17, s16, 1
	s_add_i32 s2, s12, 0xbff
	s_cmpk_lt_u32 s2, 0x37ff
	s_sext_i32_i16 s13, s13
	s_cselect_b32 s75, s63, 0xd8
	s_mul_hi_i32 s76, s13, 0x3800000
	s_mul_i32 s77, s13, 0x3800000
	s_ashr_i32 s13, s16, 1
	s_mulk_i32 s13, 0x4925
	s_lshr_b32 s16, s13, 31
	s_ashr_i32 s13, s13, 19
	s_add_i32 s13, s13, s16
	s_sext_i32_i16 s16, s13
	s_lshl_b32 s15, s15, 6
	s_lshl_b32 s16, s16, 7
	s_and_b32 s15, s15, 64
	s_or_b32 s78, s16, s15
	s_add_i32 s15, s12, 0xb801
	s_bfe_u32 s16, s15, 0x90007
	s_mulk_i32 s16, 0x2493
	s_mul_i32 s13, s13, 28
	s_lshr_b32 s16, s16, 16
	s_sub_i32 s13, s17, s13
	s_mul_i32 s17, s16, 0x380
	s_sub_i32 s15, s15, s17
	s_and_b32 s15, s15, 0xffff
	s_lshl_b32 s17, s15, 3
	s_lshl_b32 s18, s15, 6
	s_and_b32 s17, s17, 0x1f80
	s_and_b32 s18, s18, 64
	s_or_b32 s17, s17, s18
	s_add_i32 s18, s12, 0xfffff001
	s_mul_hi_i32 s19, s18, 0x92492493
	s_add_i32 s19, s19, s18
	s_lshr_b32 s20, s19, 31
	s_ashr_i32 s19, s19, 12
	s_add_i32 s19, s19, s20
	s_mulk_i32 s19, 0x1c00
	s_sub_i32 s18, s18, s19
	s_sext_i32_i16 s19, s18
	s_mulk_i32 s19, 0x4925
	s_lshr_b32 s20, s19, 31
	s_ashr_i32 s19, s19, 24
	s_add_i32 s19, s19, s20
	s_mul_i32 s20, s19, 0x380
	s_sext_i32_i16 s13, s13
	s_sub_i32 s18, s18, s20
	v_lshl_or_b32 v142, s13, 8, v157
	s_movk_i32 s13, 0x1bff
	s_lshl_b32 s15, s15, 7
	s_sext_i32_i16 s20, s18
	v_cmp_lt_i32_e64 s[40:41], s13, v142
	s_or_b32 s13, s12, 1
	s_and_b32 s15, s15, 0x700
	s_lshr_b32 s21, s20, 1
	s_addk_i32 s12, 0xc00
	s_cmpk_lt_u32 s12, 0x37ff
	s_cselect_b32 s12, s63, 0xd8
	s_ashr_i32 s20, s20, 1
	s_mulk_i32 s20, 0x4925
	s_lshr_b32 s22, s20, 31
	s_ashr_i32 s20, s20, 19
	s_add_i32 s20, s20, s22
	s_lshl_b32 s22, s20, 7
	s_lshl_b32 s18, s18, 6
	s_mul_i32 s20, s20, 28
	s_lshl_b32 s90, s27, 1
	s_and_b32 s18, s18, 64
	s_sub_i32 s20, s21, s20
	s_add_i32 s21, s90, 0x1394
	s_or_b32 s18, s22, s18
	s_mul_hi_i32 s22, s21, 0x92492493
	s_add_i32 s22, s22, s21
	s_lshr_b32 s23, s22, 31
	s_ashr_i32 s22, s22, 12
	s_add_i32 s22, s22, s23
	s_mulk_i32 s22, 0x1c00
	s_sub_i32 s21, s21, s22
	s_sext_i32_i16 s22, s21
	s_mulk_i32 s22, 0x4925
	s_lshr_b32 s23, s22, 31
	s_ashr_i32 s22, s22, 24
	s_add_i32 s22, s22, s23
	s_mul_i32 s23, s22, 0x380
	s_sub_i32 s21, s21, s23
	s_sext_i32_i16 s20, s20
	s_sext_i32_i16 s23, s21
	s_lshl_b32 s20, s20, 8
	s_lshr_b32 s24, s23, 1
	s_add_i32 s26, s90, 0x2f93
	v_ashrrev_i32_e32 v160, 2, v154
	s_cmpk_lt_u32 s26, 0x37ff
	v_add_u32_e32 v164, 0x80, v160
	s_cselect_b32 s79, s63, 0xd8
	s_ashr_i32 s23, s23, 1
	v_lshlrev_b32_e32 v2, 7, v160
	s_mulk_i32 s23, 0x4925
	v_and_b32_e32 v167, 0x7f80, v2
	v_lshlrev_b32_e32 v2, 7, v164
	s_lshr_b32 s26, s23, 31
	s_ashr_i32 s23, s23, 19
	v_and_b32_e32 v168, 0x7f80, v2
	v_lshlrev_b32_e32 v2, 15, v10
	v_lshlrev_b32_e32 v3, 1, v154
	s_add_i32 s23, s23, s26
	s_lshl_b32 s21, s21, 6
	v_and_b32_e32 v2, 0xffff0000, v2
	v_and_b32_e32 v197, 6, v3
	s_lshl_b32 s26, s23, 7
	s_and_b32 s21, s21, 64
	s_mul_i32 s23, s23, 28
	v_lshl_add_u32 v2, v11, 12, v2
	v_and_b32_e32 v3, 1, v10
	s_or_b32 s80, s26, s21
	s_sub_i32 s21, s24, s23
	v_lshl_or_b32 v2, v3, 6, v2
	s_cmpk_lt_i32 s13, 0x4800
	v_lshl_add_u32 v148, v12, 1, v2
	v_lshlrev_b32_e32 v2, 15, v13
	s_cselect_b32 s85, s12, 0xe0
	s_cselect_b32 s12, s19, s16
	v_and_b32_e32 v2, 0xffff0000, v2
	s_waitcnt vmcnt(6)
	s_movk_i32 s28, 0x1c00
	s_sext_i32_i16 s13, s21
	s_mul_hi_i32 s86, s12, 0x3800000
	s_mul_i32 s87, s12, 0x3800000
	s_cselect_b32 s12, s20, s15
	v_lshl_add_u32 v2, v14, 12, v2
	v_and_b32_e32 v3, 1, v13
	v_lshl_or_b32 v144, s13, 8, v157
	s_cselect_b32 s89, s28, 0x800
	v_or_b32_e32 v146, s12, v157
	v_lshl_or_b32 v2, v3, 6, v2
	v_and_b32_e32 v162, 48, v16
	v_lshlrev_b32_e32 v163, 6, v160
	v_lshlrev_b32_e32 v165, 6, v164
	s_mov_b32 s2, 0
	v_cmp_gt_i32_e64 s[38:39], s28, v142
	v_ashrrev_i32_e32 v143, 31, v142
	s_mul_hi_i32 s81, s22, 0x3800000
	s_mul_i32 s84, s22, 0x3800000
	v_cmp_gt_i32_e64 s[42:43], s28, v144
	v_ashrrev_i32_e32 v145, 31, v144
	v_and_b32_e32 v166, 0x7f, v160
	s_cselect_b32 s88, s18, s17
	v_cmp_gt_i32_e64 s[44:45], s89, v146
	v_ashrrev_i32_e32 v147, 31, v146
	s_lshl_b32 s16, s89, 3
	s_mov_b32 s17, s25
	s_lshl_b32 s20, s89, 4
	s_mov_b32 s21, s25
	s_mul_i32 s22, s89, 24
	s_mov_b32 s23, s25
	v_or_b32_e32 v169, s5, v18
	s_lshl_b32 s28, s89, 2
	s_mov_b32 s29, s25
	v_mov_b32_e32 v149, v130
	v_lshl_add_u32 v150, v15, 1, v2
	v_mov_b32_e32 v151, v130
	s_addk_i32 s90, 0x3393
	v_add_u32_e32 v170, 0, v20
	s_barrier
	s_branch .LBB0_2279
